# speedup vs baseline: 1.0087x; 1.0087x over previous
.LBB2_3:
	s_mul_i32 s15, s14, 0xe000
	s_add_i32 s14, s14, 1
	s_cmp_lg_u32 s14, 2
	s_cselect_b32 s14, s14, 0
	s_add_i32 s20, s15, s21
	v_add3_u32 v206, s15, v147, v148
	v_add3_u32 v207, s15, v146, v148
	s_waitcnt lgkmcnt(8)
	v_mfma_f32_16x16x32_f16 v[134:137], v[98:101], v[118:121], v[134:137]
	s_waitcnt lgkmcnt(7)
	v_mfma_f32_16x16x32_f16 v[130:133], v[90:93], v[118:121], v[130:133]
	s_waitcnt lgkmcnt(6)
	v_mfma_f32_16x16x32_f16 v[102:105], v[98:101], v[106:109], v[102:105]
	ds_read_b128 v[152:155], v206
	v_mfma_f32_16x16x32_f16 v[94:97], v[90:93], v[106:109], v[94:97]
	ds_read_b128 v[168:171], v207 offset:32768
	s_waitcnt lgkmcnt(7)
	v_mfma_f32_16x16x32_f16 v[126:129], v[82:85], v[118:121], v[126:129]
	ds_read_b128 v[172:175], v207 offset:34816
	v_mfma_f32_16x16x32_f16 v[78:81], v[82:85], v[106:109], v[78:81]
	ds_read_b128 v[156:159], v206 offset:2048
	s_waitcnt lgkmcnt(8)
	v_mfma_f32_16x16x32_f16 v[122:125], v[74:77], v[118:121], v[122:125]
	ds_read_b128 v[176:179], v207 offset:36864
	v_mfma_f32_16x16x32_f16 v[70:73], v[74:77], v[106:109], v[70:73]
	ds_read_b128 v[180:183], v207 offset:38912
	s_waitcnt lgkmcnt(9)
	v_mfma_f32_16x16x32_f16 v[54:57], v[98:101], v[86:89], v[54:57]
	ds_read_b128 v[160:163], v206 offset:4096
	v_mfma_f32_16x16x32_f16 v[46:49], v[90:93], v[86:89], v[46:49]
	ds_read_b128 v[184:187], v207 offset:40960
	v_mfma_f32_16x16x32_f16 v[42:45], v[82:85], v[86:89], v[42:45]
	ds_read_b128 v[188:191], v207 offset:43008
	v_mfma_f32_16x16x32_f16 v[38:41], v[74:77], v[86:89], v[38:41]
	ds_read_b128 v[164:167], v206 offset:6144
	s_waitcnt lgkmcnt(12)
	v_mfma_f32_16x16x32_f16 v[114:117], v[66:69], v[118:121], v[114:117]
	v_mfma_f32_16x16x32_f16 v[62:65], v[66:69], v[106:109], v[62:65]
	v_mfma_f32_16x16x32_f16 v[30:33], v[66:69], v[86:89], v[30:33]
	s_waitcnt lgkmcnt(11)
	v_mfma_f32_16x16x32_f16 v[110:113], v[50:53], v[118:121], v[110:113]
	v_mfma_f32_16x16x32_f16 v[58:61], v[50:53], v[106:109], v[58:61]
	v_mfma_f32_16x16x32_f16 v[26:29], v[50:53], v[86:89], v[26:29]
	s_waitcnt lgkmcnt(10)
	v_mfma_f32_16x16x32_f16 v[22:25], v[98:101], v[34:37], v[22:25]
	v_mfma_f32_16x16x32_f16 v[18:21], v[90:93], v[34:37], v[18:21]
	v_mfma_f32_16x16x32_f16 v[14:17], v[82:85], v[34:37], v[14:17]
	v_mfma_f32_16x16x32_f16 v[10:13], v[74:77], v[34:37], v[10:13]
	v_mfma_f32_16x16x32_f16 v[6:9], v[66:69], v[34:37], v[6:9]
	v_mfma_f32_16x16x32_f16 v[2:5], v[50:53], v[34:37], v[2:5]
	s_waitcnt vmcnt(0) lgkmcnt(0)
	s_barrier
	s_mov_b32 m0, s20
	s_mul_i32 s15, s14, 0xe000
	v_mfma_f32_16x16x32_f16 v[134:137], v[168:171], v[152:155], v[134:137]
	global_load_lds_dwordx4 v[192:193], off
	v_lshl_add_u64 v[192:193], v[192:193], 0, s[22:23]
	s_add_u32 m0, s20, 0x2000
	v_mfma_f32_16x16x32_f16 v[130:133], v[172:175], v[152:155], v[130:133]
	global_load_lds_dwordx4 v[194:195], off
	v_lshl_add_u64 v[194:195], v[194:195], 0, s[22:23]
	s_add_u32 m0, s20, 0x4000
	v_mfma_f32_16x16x32_f16 v[126:129], v[176:179], v[152:155], v[126:129]
	global_load_lds_dwordx4 v[196:197], off
	v_lshl_add_u64 v[196:197], v[196:197], 0, s[22:23]
	s_add_u32 m0, s20, 0x6000
	v_mfma_f32_16x16x32_f16 v[122:125], v[180:183], v[152:155], v[122:125]
	global_load_lds_dwordx4 v[198:199], off
	v_lshl_add_u64 v[198:199], v[198:199], 0, s[22:23]
	s_add_u32 m0, s20, 0x8000
	v_mfma_f32_16x16x32_f16 v[114:117], v[184:187], v[152:155], v[114:117]
	global_load_lds_dwordx4 v[200:201], off
	v_lshl_add_u64 v[200:201], v[200:201], 0, s[22:23]
	s_add_u32 m0, s20, 0xa000
	v_mfma_f32_16x16x32_f16 v[110:113], v[188:191], v[152:155], v[110:113]
	global_load_lds_dwordx4 v[202:203], off
	v_lshl_add_u64 v[202:203], v[202:203], 0, s[22:23]
	s_add_u32 m0, s20, 0xc000
	v_mfma_f32_16x16x32_f16 v[102:105], v[168:171], v[156:159], v[102:105]
	global_load_lds_dwordx4 v[204:205], off
	v_lshl_add_u64 v[204:205], v[204:205], 0, s[22:23]
	v_mfma_f32_16x16x32_f16 v[94:97], v[172:175], v[156:159], v[94:97]
	v_add_u32_e32 v206, s15, v150
	v_add_u32_e32 v207, s15, v151
	v_mfma_f32_16x16x32_f16 v[78:81], v[176:179], v[156:159], v[78:81]
	ds_read_b128 v[118:121], v206
	v_mfma_f32_16x16x32_f16 v[70:73], v[180:183], v[156:159], v[70:73]
	ds_read_b128 v[98:101], v207 offset:32768
	v_mfma_f32_16x16x32_f16 v[62:65], v[184:187], v[156:159], v[62:65]
	ds_read_b128 v[90:93], v207 offset:34816
	v_mfma_f32_16x16x32_f16 v[58:61], v[188:191], v[156:159], v[58:61]
	ds_read_b128 v[106:109], v206 offset:2048
	v_mfma_f32_16x16x32_f16 v[54:57], v[168:171], v[160:163], v[54:57]
	ds_read_b128 v[82:85], v207 offset:36864
	v_mfma_f32_16x16x32_f16 v[46:49], v[172:175], v[160:163], v[46:49]
	ds_read_b128 v[74:77], v207 offset:38912
	v_mfma_f32_16x16x32_f16 v[42:45], v[176:179], v[160:163], v[42:45]
	ds_read_b128 v[86:89], v206 offset:4096
	v_mfma_f32_16x16x32_f16 v[38:41], v[180:183], v[160:163], v[38:41]
	ds_read_b128 v[66:69], v207 offset:40960
	v_mfma_f32_16x16x32_f16 v[30:33], v[184:187], v[160:163], v[30:33]
	ds_read_b128 v[50:53], v207 offset:43008
	v_mfma_f32_16x16x32_f16 v[26:29], v[188:191], v[160:163], v[26:29]
	ds_read_b128 v[34:37], v206 offset:6144
	v_mfma_f32_16x16x32_f16 v[22:25], v[168:171], v[164:167], v[22:25]
	v_mfma_f32_16x16x32_f16 v[18:21], v[172:175], v[164:167], v[18:21]
	v_mfma_f32_16x16x32_f16 v[14:17], v[176:179], v[164:167], v[14:17]
	v_mfma_f32_16x16x32_f16 v[10:13], v[180:183], v[164:167], v[10:13]
	v_mfma_f32_16x16x32_f16 v[6:9], v[184:187], v[164:167], v[6:9]
	v_mfma_f32_16x16x32_f16 v[2:5], v[188:191], v[164:167], v[2:5]
	s_add_u32 s0, s0, 0x80
	s_addc_u32 s1, s1, 0
	s_cmpk_eq_i32 s0, 0x700
	s_cbranch_scc0 .LBB2_3
	s_add_i32 s0, s15, 0
	v_add3_u32 v0, s0, v147, v148
	s_waitcnt lgkmcnt(0)
	v_mfma_f32_16x16x32_f16 v[134:137], v[98:101], v[118:121], v[134:137]
	s_add_i32 s1, s14, 1
	s_cmp_lg_u32 s1, 2
	s_cselect_b32 s1, s1, 0
	v_mfma_f32_16x16x32_f16 v[130:133], v[90:93], v[118:121], v[130:133]
	v_mfma_f32_16x16x32_f16 v[126:129], v[82:85], v[118:121], v[126:129]
	v_mfma_f32_16x16x32_f16 v[102:105], v[98:101], v[106:109], v[102:105]
	v_mfma_f32_16x16x32_f16 v[94:97], v[90:93], v[106:109], v[94:97]
	v_mfma_f32_16x16x32_f16 v[78:81], v[82:85], v[106:109], v[78:81]
	v_mfma_f32_16x16x32_f16 v[54:57], v[98:101], v[86:89], v[54:57]
	v_mfma_f32_16x16x32_f16 v[46:49], v[90:93], v[86:89], v[46:49]
	v_mfma_f32_16x16x32_f16 v[42:45], v[82:85], v[86:89], v[42:45]
	v_mfma_f32_16x16x32_f16 v[38:41], v[74:77], v[86:89], v[38:41]
	v_mfma_f32_16x16x32_f16 v[30:33], v[66:69], v[86:89], v[30:33]
	v_mfma_f32_16x16x32_f16 v[26:29], v[50:53], v[86:89], v[26:29]
	v_mfma_f32_16x16x32_f16 v[22:25], v[98:101], v[34:37], v[22:25]
	v_mfma_f32_16x16x32_f16 v[18:21], v[90:93], v[34:37], v[18:21]
	ds_read_b128 v[86:89], v0
	ds_read_b128 v[90:93], v0 offset:2048
	v_mfma_f32_16x16x32_f16 v[14:17], v[82:85], v[34:37], v[14:17]
	ds_read_b128 v[82:85], v0 offset:4096
	ds_read_b128 v[98:101], v0 offset:6144
	v_add3_u32 v0, s0, v146, v148
	v_mfma_f32_16x16x32_f16 v[122:125], v[74:77], v[118:121], v[122:125]
	v_mfma_f32_16x16x32_f16 v[114:117], v[66:69], v[118:121], v[114:117]
	v_mfma_f32_16x16x32_f16 v[110:113], v[50:53], v[118:121], v[110:113]
	v_mfma_f32_16x16x32_f16 v[70:73], v[74:77], v[106:109], v[70:73]
	v_mfma_f32_16x16x32_f16 v[62:65], v[66:69], v[106:109], v[62:65]
	v_mfma_f32_16x16x32_f16 v[58:61], v[50:53], v[106:109], v[58:61]
	v_mfma_f32_16x16x32_f16 v[10:13], v[74:77], v[34:37], v[10:13]
	ds_read_b128 v[74:77], v0 offset:32768
	ds_read_b128 v[106:109], v0 offset:34816
	v_mfma_f32_16x16x32_f16 v[6:9], v[66:69], v[34:37], v[6:9]
	ds_read_b128 v[66:69], v0 offset:36864
	ds_read_b128 v[118:121], v0 offset:38912
	ds_read_b128 v[152:155], v0 offset:40960
	ds_read_b128 v[156:159], v0 offset:43008
	v_mfma_f32_16x16x32_f16 v[0:3], v[50:53], v[34:37], v[2:5]
	s_mul_i32 s1, s1, 0xe000
	s_waitcnt vmcnt(0) lgkmcnt(0)
	s_barrier
	v_add_u32_e32 v4, s1, v150
	ds_read_b128 v[34:37], v4
	ds_read_b128 v[50:53], v4 offset:2048
	ds_read_b128 v[160:163], v4 offset:4096
	ds_read_b128 v[164:167], v4 offset:6144
	v_add_u32_e32 v4, s1, v151
	ds_read_b128 v[168:171], v4 offset:32768
	ds_read_b128 v[172:175], v4 offset:34816
	ds_read_b128 v[176:179], v4 offset:36864
	ds_read_b128 v[180:183], v4 offset:38912
	ds_read_b128 v[184:187], v4 offset:40960
	ds_read_b128 v[188:191], v4 offset:43008
	v_mfma_f32_16x16x32_f16 v[134:137], v[74:77], v[86:89], v[134:137]
	v_mfma_f32_16x16x32_f16 v[130:133], v[106:109], v[86:89], v[130:133]
	v_mfma_f32_16x16x32_f16 v[126:129], v[66:69], v[86:89], v[126:129]
	v_mfma_f32_16x16x32_f16 v[122:125], v[118:121], v[86:89], v[122:125]
	v_mfma_f32_16x16x32_f16 v[114:117], v[152:155], v[86:89], v[114:117]
	v_mfma_f32_16x16x32_f16 v[86:89], v[156:159], v[86:89], v[110:113]
	v_mfma_f32_16x16x32_f16 v[102:105], v[74:77], v[90:93], v[102:105]
	v_mfma_f32_16x16x32_f16 v[94:97], v[106:109], v[90:93], v[94:97]
	v_mfma_f32_16x16x32_f16 v[78:81], v[66:69], v[90:93], v[78:81]
	v_mfma_f32_16x16x32_f16 v[70:73], v[118:121], v[90:93], v[70:73]
	v_mfma_f32_16x16x32_f16 v[62:65], v[152:155], v[90:93], v[62:65]
	v_mfma_f32_16x16x32_f16 v[58:61], v[156:159], v[90:93], v[58:61]
	v_mfma_f32_16x16x32_f16 v[54:57], v[74:77], v[82:85], v[54:57]
	v_mfma_f32_16x16x32_f16 v[46:49], v[106:109], v[82:85], v[46:49]
	v_mfma_f32_16x16x32_f16 v[42:45], v[66:69], v[82:85], v[42:45]
	v_mfma_f32_16x16x32_f16 v[38:41], v[118:121], v[82:85], v[38:41]
	v_mfma_f32_16x16x32_f16 v[30:33], v[152:155], v[82:85], v[30:33]
	v_mfma_f32_16x16x32_f16 v[26:29], v[156:159], v[82:85], v[26:29]
	v_mfma_f32_16x16x32_f16 v[22:25], v[74:77], v[98:101], v[22:25]
	v_mfma_f32_16x16x32_f16 v[18:21], v[106:109], v[98:101], v[18:21]
	v_mfma_f32_16x16x32_f16 v[14:17], v[66:69], v[98:101], v[14:17]
	v_mfma_f32_16x16x32_f16 v[10:13], v[118:121], v[98:101], v[10:13]
	v_mfma_f32_16x16x32_f16 v[4:7], v[152:155], v[98:101], v[6:9]
	v_mfma_f32_16x16x32_f16 v[0:3], v[156:159], v[98:101], v[0:3]
	s_add_i32 s0, s1, 0
	s_nop 0
	v_add3_u32 v8, s0, v147, v148
	s_waitcnt lgkmcnt(5)
	v_mfma_f32_16x16x32_f16 v[66:69], v[168:171], v[34:37], v[134:137]
	s_waitcnt lgkmcnt(4)
	v_mfma_f32_16x16x32_f16 v[74:77], v[172:175], v[34:37], v[130:133]
	s_waitcnt lgkmcnt(3)
	v_mfma_f32_16x16x32_f16 v[82:85], v[176:179], v[34:37], v[126:129]
	s_waitcnt lgkmcnt(2)
	v_mfma_f32_16x16x32_f16 v[90:93], v[180:183], v[34:37], v[122:125]
	s_waitcnt lgkmcnt(1)
	v_mfma_f32_16x16x32_f16 v[98:101], v[184:187], v[34:37], v[114:117]
	s_waitcnt lgkmcnt(0)
	v_mfma_f32_16x16x32_f16 v[34:37], v[188:191], v[34:37], v[86:89]
	v_mfma_f32_16x16x32_f16 v[86:89], v[168:171], v[50:53], v[102:105]
	v_mfma_f32_16x16x32_f16 v[94:97], v[172:175], v[50:53], v[94:97]
	v_mfma_f32_16x16x32_f16 v[78:81], v[176:179], v[50:53], v[78:81]
	v_mfma_f32_16x16x32_f16 v[70:73], v[180:183], v[50:53], v[70:73]
	v_mfma_f32_16x16x32_f16 v[62:65], v[184:187], v[50:53], v[62:65]
	v_mfma_f32_16x16x32_f16 v[50:53], v[188:191], v[50:53], v[58:61]
	s_nop 2
	ds_read_b128 v[58:61], v8
	ds_read_b128 v[102:105], v8 offset:2048
	ds_read_b128 v[106:109], v8 offset:4096
	ds_read_b128 v[110:113], v8 offset:6144
	v_mfma_f32_16x16x32_f16 v[8:11], v[180:183], v[164:167], v[10:13]
	s_nop 2
	v_add3_u32 v12, s0, v146, v148
	ds_read_b128 v[114:117], v12 offset:32768
	ds_read_b128 v[118:121], v12 offset:34816
	ds_read_b128 v[122:125], v12 offset:36864
	ds_read_b128 v[126:129], v12 offset:38912
	ds_read_b128 v[130:133], v12 offset:40960
	ds_read_b128 v[134:137], v12 offset:43008
	v_mfma_f32_16x16x32_f16 v[54:57], v[168:171], v[160:163], v[54:57]
	v_mfma_f32_16x16x32_f16 v[46:49], v[172:175], v[160:163], v[46:49]
	v_mfma_f32_16x16x32_f16 v[42:45], v[176:179], v[160:163], v[42:45]
	v_mfma_f32_16x16x32_f16 v[38:41], v[180:183], v[160:163], v[38:41]
	v_mfma_f32_16x16x32_f16 v[30:33], v[184:187], v[160:163], v[30:33]
	v_mfma_f32_16x16x32_f16 v[26:29], v[188:191], v[160:163], v[26:29]
	v_mfma_f32_16x16x32_f16 v[22:25], v[168:171], v[164:167], v[22:25]
	v_mfma_f32_16x16x32_f16 v[18:21], v[172:175], v[164:167], v[18:21]
	v_mfma_f32_16x16x32_f16 v[14:17], v[176:179], v[164:167], v[14:17]
	v_mfma_f32_16x16x32_f16 v[4:7], v[184:187], v[164:167], v[4:7]
	v_mfma_f32_16x16x32_f16 v[0:3], v[188:191], v[164:167], v[0:3]
	s_waitcnt vmcnt(0) lgkmcnt(0)
	s_barrier
	v_mfma_f32_16x16x32_f16 v[66:69], v[114:117], v[58:61], v[66:69]
	v_mfma_f32_16x16x32_f16 v[74:77], v[118:121], v[58:61], v[74:77]
	v_mfma_f32_16x16x32_f16 v[82:85], v[122:125], v[58:61], v[82:85]
	v_mfma_f32_16x16x32_f16 v[90:93], v[126:129], v[58:61], v[90:93]
	v_mfma_f32_16x16x32_f16 v[98:101], v[130:133], v[58:61], v[98:101]
	v_mfma_f32_16x16x32_f16 v[34:37], v[134:137], v[58:61], v[34:37]
	v_mfma_f32_16x16x32_f16 v[58:61], v[114:117], v[102:105], v[86:89]
	v_mfma_f32_16x16x32_f16 v[86:89], v[118:121], v[102:105], v[94:97]
	v_mfma_f32_16x16x32_f16 v[78:81], v[122:125], v[102:105], v[78:81]
	v_mfma_f32_16x16x32_f16 v[70:73], v[126:129], v[102:105], v[70:73]
	v_mfma_f32_16x16x32_f16 v[62:65], v[130:133], v[102:105], v[62:65]
	v_mfma_f32_16x16x32_f16 v[50:53], v[134:137], v[102:105], v[50:53]
	v_mfma_f32_16x16x32_f16 v[54:57], v[114:117], v[106:109], v[54:57]
	v_mfma_f32_16x16x32_f16 v[46:49], v[118:121], v[106:109], v[46:49]
	v_mfma_f32_16x16x32_f16 v[42:45], v[122:125], v[106:109], v[42:45]
	v_mfma_f32_16x16x32_f16 v[38:41], v[126:129], v[106:109], v[38:41]
	v_mfma_f32_16x16x32_f16 v[30:33], v[130:133], v[106:109], v[30:33]
	v_mfma_f32_16x16x32_f16 v[26:29], v[134:137], v[106:109], v[26:29]
	v_mfma_f32_16x16x32_f16 v[22:25], v[114:117], v[110:113], v[22:25]
	v_mfma_f32_16x16x32_f16 v[18:21], v[118:121], v[110:113], v[18:21]
	v_mfma_f32_16x16x32_f16 v[12:15], v[122:125], v[110:113], v[14:17]
	v_mfma_f32_16x16x32_f16 v[8:11], v[126:129], v[110:113], v[8:11]
	v_mfma_f32_16x16x32_f16 v[4:7], v[130:133], v[110:113], v[4:7]
	v_mfma_f32_16x16x32_f16 v[0:3], v[134:137], v[110:113], v[0:3]
	s_movk_i32 s0, 0x3400
	v_mad_u32_u24 v94, v144, s0, 0
	v_lshlrev_b32_e32 v16, 3, v145
	v_mul_u32_u24_e32 v17, 0xd0, v143
	v_add3_u32 v95, v94, v16, v17
	v_cvt_pk_f16_f32 v17, v68, v69
	v_cvt_pk_f16_f32 v16, v66, v67
	v_cvt_pk_f16_f32 v67, v76, v77
	v_cvt_pk_f16_f32 v66, v74, v75
	s_barrier
	ds_write2_b64 v95, v[16:17], v[66:67] offset1:4
	v_cvt_pk_f16_f32 v17, v84, v85
	v_cvt_pk_f16_f32 v16, v82, v83
	v_cvt_pk_f16_f32 v67, v92, v93
	v_cvt_pk_f16_f32 v66, v90, v91
	s_mov_b32 s0, 0x15555556
	ds_write2_b64 v95, v[16:17], v[66:67] offset0:8 offset1:12
	v_cvt_pk_f16_f32 v17, v100, v101
	v_cvt_pk_f16_f32 v16, v98, v99
	v_cvt_pk_f16_f32 v37, v36, v37
	v_cvt_pk_f16_f32 v36, v34, v35
	v_cvt_pk_f16_f32 v7, v6, v7
	v_cvt_pk_f16_f32 v6, v4, v5
	v_mul_hi_u32 v4, v140, s0
	ds_write2_b64 v95, v[16:17], v[36:37] offset0:16 offset1:20
	v_cvt_pk_f16_f32 v17, v60, v61
	v_cvt_pk_f16_f32 v16, v58, v59
	v_cvt_pk_f16_f32 v35, v88, v89
	v_cvt_pk_f16_f32 v34, v86, v87
	v_add_u32_e32 v36, 0x800, v95
	v_cvt_pk_f16_f32 v21, v20, v21
	v_cvt_pk_f16_f32 v20, v18, v19
	v_add_u32_e32 v18, 0x2000, v95
	v_cvt_pk_f16_f32 v15, v14, v15
	v_cvt_pk_f16_f32 v14, v12, v13
	v_cvt_pk_f16_f32 v11, v10, v11
	v_cvt_pk_f16_f32 v10, v8, v9
	v_cvt_pk_f16_f32 v3, v2, v3
	v_cvt_pk_f16_f32 v2, v0, v1
	v_mul_u32_u24_e32 v0, 12, v4
	ds_write2_b64 v36, v[16:17], v[34:35] offset0:160 offset1:164
	v_cvt_pk_f16_f32 v17, v80, v81
	v_cvt_pk_f16_f32 v16, v78, v79
	v_cvt_pk_f16_f32 v35, v72, v73
	v_cvt_pk_f16_f32 v34, v70, v71
	ds_write2_b64 v18, v[14:15], v[10:11] offset0:232 offset1:236
	v_add_u32_e32 v10, s13, v142
	v_sub_u32_e32 v5, v140, v0
	ds_write2_b64 v36, v[16:17], v[34:35] offset0:168 offset1:172
	v_cvt_pk_f16_f32 v17, v64, v65
	v_cvt_pk_f16_f32 v16, v62, v63
	v_cvt_pk_f16_f32 v35, v52, v53
	v_cvt_pk_f16_f32 v34, v50, v51
	v_lshl_add_u32 v12, v5, 3, v10
	ds_write2_b64 v36, v[16:17], v[34:35] offset0:176 offset1:180
	v_cvt_pk_f16_f32 v17, v56, v57
	v_cvt_pk_f16_f32 v16, v54, v55
	v_cvt_pk_f16_f32 v35, v48, v49
	v_cvt_pk_f16_f32 v34, v46, v47
	v_add_u32_e32 v36, 0x1800, v95
	v_lshrrev_b32_e32 v0, 10, v12
	v_mov_b32_e32 v1, 0
	ds_write2_b64 v36, v[16:17], v[34:35] offset0:64 offset1:68
	v_cvt_pk_f16_f32 v17, v44, v45
	v_cvt_pk_f16_f32 v16, v42, v43
	v_cvt_pk_f16_f32 v35, v40, v41
	v_cvt_pk_f16_f32 v34, v38, v39
	ds_write2_b64 v18, v[6:7], v[2:3] offset0:240 offset1:244
	v_add_u32_e32 v11, s12, v141
	v_lshlrev_b64 v[2:3], 23, v[0:1]
	ds_write2_b64 v36, v[16:17], v[34:35] offset0:72 offset1:76
	v_cvt_pk_f16_f32 v17, v32, v33
	v_cvt_pk_f16_f32 v16, v30, v31
	v_cvt_pk_f16_f32 v29, v28, v29
	v_cvt_pk_f16_f32 v28, v26, v27
	v_lshl_add_u64 v[6:7], s[8:9], 0, v[2:3]
	v_or_b32_e32 v2, v11, v4
	ds_write2_b64 v36, v[16:17], v[28:29] offset0:80 offset1:84
	v_cvt_pk_f16_f32 v17, v24, v25
	v_cvt_pk_f16_f32 v16, v22, v23
	v_ashrrev_i32_e32 v3, 31, v2
	ds_write2_b64 v18, v[16:17], v[20:21] offset0:224 offset1:228
	v_lshlrev_b64 v[8:9], 11, v[2:3]
	v_mul_u32_u24_e32 v0, 0xd0, v4
	v_lshlrev_b32_e32 v2, 4, v5
	s_waitcnt lgkmcnt(0)
	v_add3_u32 v0, v94, v0, v2
	ds_read_b128 v[2:5], v0
	v_and_b32_e32 v0, 0x3f8, v12
	v_lshl_add_u64 v[6:7], v[6:7], 0, v[8:9]
	v_lshlrev_b32_e32 v0, 1, v0
	v_lshl_add_u64 v[6:7], v[6:7], 0, v[0:1]
	v_or_b32_e32 v0, 64, v140
	s_waitcnt lgkmcnt(0)
	global_store_dwordx4 v[6:7], v[2:5], off sc1
	s_nop 1
	v_mul_hi_u32 v4, v0, s0
	v_mul_u32_u24_e32 v2, 12, v4
	v_sub_u32_e32 v5, v0, v2
	v_lshl_add_u32 v12, v5, 3, v10
	v_lshrrev_b32_e32 v0, 10, v12
	v_lshlrev_b64 v[2:3], 23, v[0:1]
	v_lshl_add_u64 v[6:7], s[8:9], 0, v[2:3]
	v_or_b32_e32 v2, v11, v4
	v_ashrrev_i32_e32 v3, 31, v2
	v_lshlrev_b64 v[8:9], 11, v[2:3]
	v_mul_u32_u24_e32 v0, 0xd0, v4
	v_lshlrev_b32_e32 v2, 4, v5
	v_add3_u32 v0, v94, v0, v2
	ds_read_b128 v[2:5], v0
	v_and_b32_e32 v0, 0x3f8, v12
	v_lshl_add_u64 v[6:7], v[6:7], 0, v[8:9]
	v_lshlrev_b32_e32 v0, 1, v0
	v_lshl_add_u64 v[6:7], v[6:7], 0, v[0:1]
	v_or_b32_e32 v0, 0x80, v140
	s_waitcnt lgkmcnt(0)
	global_store_dwordx4 v[6:7], v[2:5], off sc1
	s_nop 1
	v_mul_hi_u32 v4, v0, s0
	v_mul_u32_u24_e32 v2, 12, v4
	v_sub_u32_e32 v5, v0, v2
	v_lshl_add_u32 v12, v5, 3, v10
	v_lshrrev_b32_e32 v0, 10, v12
	v_lshlrev_b64 v[2:3], 23, v[0:1]
	v_lshl_add_u64 v[6:7], s[8:9], 0, v[2:3]
	v_or_b32_e32 v2, v11, v4
	v_ashrrev_i32_e32 v3, 31, v2
	v_lshlrev_b64 v[8:9], 11, v[2:3]
	v_mul_u32_u24_e32 v0, 0xd0, v4
	v_lshlrev_b32_e32 v2, 4, v5
	v_add3_u32 v0, v94, v0, v2
	ds_read_b128 v[2:5], v0
	v_and_b32_e32 v0, 0x3f8, v12
	v_lshl_add_u64 v[6:7], v[6:7], 0, v[8:9]
	v_lshlrev_b32_e32 v0, 1, v0
	v_lshl_add_u64 v[6:7], v[6:7], 0, v[0:1]
	v_or_b32_e32 v0, 0xc0, v140
	s_waitcnt lgkmcnt(0)
	global_store_dwordx4 v[6:7], v[2:5], off sc1
	s_nop 1
	v_mul_hi_u32 v4, v0, s0
	v_mul_u32_u24_e32 v2, 12, v4
	v_sub_u32_e32 v5, v0, v2
	v_lshl_add_u32 v12, v5, 3, v10
	v_lshrrev_b32_e32 v0, 10, v12
	v_lshlrev_b64 v[2:3], 23, v[0:1]
	v_lshl_add_u64 v[6:7], s[8:9], 0, v[2:3]
	v_or_b32_e32 v2, v11, v4
	v_ashrrev_i32_e32 v3, 31, v2
	v_lshlrev_b64 v[8:9], 11, v[2:3]
	v_mul_u32_u24_e32 v0, 0xd0, v4
	v_lshlrev_b32_e32 v2, 4, v5
	v_add3_u32 v0, v94, v0, v2
	ds_read_b128 v[2:5], v0
	v_and_b32_e32 v0, 0x3f8, v12
	v_lshl_add_u64 v[6:7], v[6:7], 0, v[8:9]
	v_lshlrev_b32_e32 v0, 1, v0
	v_lshl_add_u64 v[6:7], v[6:7], 0, v[0:1]
	v_or_b32_e32 v0, 0x100, v140
	s_waitcnt lgkmcnt(0)
	global_store_dwordx4 v[6:7], v[2:5], off sc1
	s_nop 1
	v_mul_hi_u32 v4, v0, s0
	v_mul_u32_u24_e32 v2, 12, v4
	v_sub_u32_e32 v5, v0, v2
	v_lshl_add_u32 v12, v5, 3, v10
	v_lshrrev_b32_e32 v0, 10, v12
	v_lshlrev_b64 v[2:3], 23, v[0:1]
	v_lshl_add_u64 v[6:7], s[8:9], 0, v[2:3]
	v_or_b32_e32 v2, v11, v4
	v_ashrrev_i32_e32 v3, 31, v2
	v_lshlrev_b64 v[8:9], 11, v[2:3]
	v_mul_u32_u24_e32 v0, 0xd0, v4
	v_lshlrev_b32_e32 v2, 4, v5
	v_add3_u32 v0, v94, v0, v2
	ds_read_b128 v[2:5], v0
	v_and_b32_e32 v0, 0x3f8, v12
	v_lshl_add_u64 v[6:7], v[6:7], 0, v[8:9]
	v_lshlrev_b32_e32 v0, 1, v0
	v_lshl_add_u64 v[6:7], v[6:7], 0, v[0:1]
	v_or_b32_e32 v0, 0x140, v140
	s_waitcnt lgkmcnt(0)
	global_store_dwordx4 v[6:7], v[2:5], off sc1
	s_nop 1
	v_mul_hi_u32 v4, v0, s0
	v_mul_u32_u24_e32 v2, 12, v4
	v_sub_u32_e32 v5, v0, v2
	v_lshl_add_u32 v12, v5, 3, v10
	v_lshrrev_b32_e32 v0, 10, v12
	v_lshlrev_b64 v[2:3], 23, v[0:1]
	v_lshl_add_u64 v[6:7], s[8:9], 0, v[2:3]
	v_or_b32_e32 v2, v11, v4
	v_ashrrev_i32_e32 v3, 31, v2
	v_lshlrev_b64 v[8:9], 11, v[2:3]
	v_mul_u32_u24_e32 v0, 0xd0, v4
	v_lshlrev_b32_e32 v2, 4, v5
	v_add3_u32 v0, v94, v0, v2
	ds_read_b128 v[2:5], v0
	v_and_b32_e32 v0, 0x3f8, v12
	v_lshl_add_u64 v[6:7], v[6:7], 0, v[8:9]
	v_lshlrev_b32_e32 v0, 1, v0
	v_lshl_add_u64 v[6:7], v[6:7], 0, v[0:1]
	v_or_b32_e32 v0, 0x180, v140
	s_waitcnt lgkmcnt(0)
	global_store_dwordx4 v[6:7], v[2:5], off sc1
	s_nop 1
	v_mul_hi_u32 v4, v0, s0
	v_mul_u32_u24_e32 v2, 12, v4
	v_sub_u32_e32 v5, v0, v2
	v_lshl_add_u32 v12, v5, 3, v10
	v_lshrrev_b32_e32 v0, 10, v12
	v_lshlrev_b64 v[2:3], 23, v[0:1]
	v_lshl_add_u64 v[6:7], s[8:9], 0, v[2:3]
	v_or_b32_e32 v2, v11, v4
	v_ashrrev_i32_e32 v3, 31, v2
	v_lshlrev_b64 v[8:9], 11, v[2:3]
	v_mul_u32_u24_e32 v0, 0xd0, v4
	v_lshlrev_b32_e32 v2, 4, v5
	v_add3_u32 v0, v94, v0, v2
	ds_read_b128 v[2:5], v0
	v_and_b32_e32 v0, 0x3f8, v12
	v_lshl_add_u64 v[6:7], v[6:7], 0, v[8:9]
	v_lshlrev_b32_e32 v0, 1, v0
	v_lshl_add_u64 v[6:7], v[6:7], 0, v[0:1]
	v_or_b32_e32 v0, 0x1c0, v140
	s_waitcnt lgkmcnt(0)
	global_store_dwordx4 v[6:7], v[2:5], off sc1
	s_nop 1
	v_mul_hi_u32 v4, v0, s0
	v_mul_u32_u24_e32 v2, 12, v4
	v_sub_u32_e32 v5, v0, v2
	v_lshl_add_u32 v12, v5, 3, v10
	v_lshrrev_b32_e32 v0, 10, v12
	v_lshlrev_b64 v[2:3], 23, v[0:1]
	v_lshl_add_u64 v[6:7], s[8:9], 0, v[2:3]
	v_or_b32_e32 v2, v11, v4
	v_ashrrev_i32_e32 v3, 31, v2
	v_lshlrev_b64 v[8:9], 11, v[2:3]
	v_mul_u32_u24_e32 v0, 0xd0, v4
	v_lshlrev_b32_e32 v2, 4, v5
	v_add3_u32 v0, v94, v0, v2
	ds_read_b128 v[2:5], v0
	v_and_b32_e32 v0, 0x3f8, v12
	v_lshl_add_u64 v[6:7], v[6:7], 0, v[8:9]
	v_lshlrev_b32_e32 v0, 1, v0
	v_lshl_add_u64 v[6:7], v[6:7], 0, v[0:1]
	v_or_b32_e32 v0, 0x200, v140
	s_waitcnt lgkmcnt(0)
	global_store_dwordx4 v[6:7], v[2:5], off sc1
	s_nop 1
	v_mul_hi_u32 v4, v0, s0
	v_mul_u32_u24_e32 v2, 12, v4
	v_sub_u32_e32 v5, v0, v2
	v_lshl_add_u32 v12, v5, 3, v10
	v_lshrrev_b32_e32 v0, 10, v12
	v_lshlrev_b64 v[2:3], 23, v[0:1]
	v_lshl_add_u64 v[6:7], s[8:9], 0, v[2:3]
	v_or_b32_e32 v2, v11, v4
	v_ashrrev_i32_e32 v3, 31, v2
	v_lshlrev_b64 v[8:9], 11, v[2:3]
	v_mul_u32_u24_e32 v0, 0xd0, v4
	v_lshlrev_b32_e32 v2, 4, v5
	v_add3_u32 v0, v94, v0, v2
	ds_read_b128 v[2:5], v0
	v_and_b32_e32 v0, 0x3f8, v12
	v_lshl_add_u64 v[6:7], v[6:7], 0, v[8:9]
	v_lshlrev_b32_e32 v0, 1, v0
	v_lshl_add_u64 v[6:7], v[6:7], 0, v[0:1]
	v_or_b32_e32 v0, 0x240, v140
	s_waitcnt lgkmcnt(0)
	global_store_dwordx4 v[6:7], v[2:5], off sc1
	s_nop 1
	v_mul_hi_u32 v4, v0, s0
	v_mul_u32_u24_e32 v2, 12, v4
	v_sub_u32_e32 v5, v0, v2
	v_lshl_add_u32 v12, v5, 3, v10
	v_lshrrev_b32_e32 v0, 10, v12
	v_lshlrev_b64 v[2:3], 23, v[0:1]
	v_lshl_add_u64 v[6:7], s[8:9], 0, v[2:3]
	v_or_b32_e32 v2, v11, v4
	v_ashrrev_i32_e32 v3, 31, v2
	v_lshlrev_b64 v[8:9], 11, v[2:3]
	v_mul_u32_u24_e32 v0, 0xd0, v4
	v_lshlrev_b32_e32 v2, 4, v5
	v_add3_u32 v0, v94, v0, v2
	ds_read_b128 v[2:5], v0
	v_and_b32_e32 v0, 0x3f8, v12
	v_lshl_add_u64 v[6:7], v[6:7], 0, v[8:9]
	v_lshlrev_b32_e32 v0, 1, v0
	v_lshl_add_u64 v[6:7], v[6:7], 0, v[0:1]
	v_or_b32_e32 v0, 0x280, v140
	s_waitcnt lgkmcnt(0)
	global_store_dwordx4 v[6:7], v[2:5], off sc1
	s_nop 1
	v_mul_hi_u32 v4, v0, s0
	v_mul_u32_u24_e32 v2, 12, v4
	v_sub_u32_e32 v5, v0, v2
	v_lshl_add_u32 v12, v5, 3, v10
	v_lshrrev_b32_e32 v0, 10, v12
	v_lshlrev_b64 v[2:3], 23, v[0:1]
	v_lshl_add_u64 v[6:7], s[8:9], 0, v[2:3]
	v_or_b32_e32 v2, v11, v4
	v_ashrrev_i32_e32 v3, 31, v2
	v_lshlrev_b64 v[8:9], 11, v[2:3]
	v_mul_u32_u24_e32 v0, 0xd0, v4
	v_lshlrev_b32_e32 v2, 4, v5
	v_add3_u32 v0, v94, v0, v2
	ds_read_b128 v[2:5], v0
	v_and_b32_e32 v0, 0x3f8, v12
	v_lshl_add_u64 v[6:7], v[6:7], 0, v[8:9]
	v_lshlrev_b32_e32 v0, 1, v0
	v_lshl_add_u64 v[6:7], v[6:7], 0, v[0:1]
	v_or_b32_e32 v0, 0x2c0, v140
	s_waitcnt lgkmcnt(0)
	global_store_dwordx4 v[6:7], v[2:5], off sc1
	s_nop 1
	v_mul_hi_u32 v4, v0, s0
	v_mul_u32_u24_e32 v2, 12, v4
	v_sub_u32_e32 v5, v0, v2
	v_lshl_add_u32 v10, v5, 3, v10
	v_lshrrev_b32_e32 v0, 10, v10
	v_lshlrev_b64 v[2:3], 23, v[0:1]
	v_lshl_add_u64 v[6:7], s[8:9], 0, v[2:3]
	v_or_b32_e32 v2, v11, v4
	v_ashrrev_i32_e32 v3, 31, v2
	v_lshlrev_b64 v[8:9], 11, v[2:3]
	v_mul_u32_u24_e32 v0, 0xd0, v4
	v_lshlrev_b32_e32 v2, 4, v5
	v_add3_u32 v0, v94, v0, v2
	ds_read_b128 v[2:5], v0
	v_and_b32_e32 v0, 0x3f8, v10
	v_lshl_add_u64 v[6:7], v[6:7], 0, v[8:9]
	v_lshlrev_b32_e32 v0, 1, v0
	v_lshl_add_u64 v[0:1], v[6:7], 0, v[0:1]
	s_waitcnt lgkmcnt(0)
	global_store_dwordx4 v[0:1], v[2:5], off sc1
	s_nop 1
	s_endpgm
	s_nop 0
	s_nop 0
	s_nop 0
	s_nop 0
	s_nop 0
	s_nop 0
	s_nop 0
	s_nop 0
	s_nop 0
	s_nop 0
	s_nop 0
	s_nop 0
	s_nop 0
	s_nop 0
	s_nop 0
	s_nop 0
	s_nop 0
	s_nop 0
	s_nop 0
	s_nop 0
	s_nop 0
	s_nop 0
	s_nop 0
	s_nop 0
	s_nop 0
	s_nop 0
	s_nop 0
	s_nop 0
	s_nop 0
	s_nop 0
	s_nop 0
	s_nop 0
	s_nop 0
	s_nop 0
	s_nop 0
	s_nop 0
	s_nop 0
	s_nop 0
	s_nop 0
	s_nop 0
	s_nop 0
	s_nop 0
	s_nop 0
	s_nop 0
	s_nop 0
	s_nop 0
	s_nop 0
	s_nop 0
	s_endpgm
